# speedup vs baseline: 1.0441x; 1.0042x over previous
.LBB4_18:
.LBB4_24:
	s_and_b64 s[50:51], s[42:43], exec
	s_cselect_b32 s52, s39, s47
	s_cselect_b32 s53, s38, s46
	s_cselect_b32 s54, s41, s45
	s_cselect_b32 s55, s40, s44
	s_add_u32 s28, s46, 0x100
	s_addc_u32 s84, s47, 0
	s_and_b64 s[50:51], s[48:49], exec
	s_cselect_b32 s51, s52, s84
	s_cselect_b32 s50, s53, s28
	s_add_u32 s28, s44, 0x100
	s_addc_u32 s84, s45, 0
	s_and_b64 s[48:49], s[48:49], exec
	s_cselect_b32 s49, s54, s84
	s_cselect_b32 s48, s55, s28
	s_mov_b32 m0, s59
	v_add_u32_e32 v229, s76, v234
	v_lshl_add_u64 v[130:131], s[48:49], 0, v[216:217]
	ds_read_b128 v[74:77], v229
	ds_read_b128 v[86:89], v229 offset:1024
	ds_read_b128 v[98:101], v229 offset:2048
	ds_read_b128 v[106:109], v229 offset:3072
	global_load_lds_dwordx4 v[130:131], off
	v_lshl_add_u64 v[132:133], s[48:49], 0, v[218:219]
	s_mov_b32 m0, s60
	s_nop 0
	global_load_lds_dwordx4 v[132:133], off
	s_barrier
	s_waitcnt lgkmcnt(0)
	s_setprio 1
	s_waitcnt lgkmcnt(0)
	v_mfma_f32_16x16x32_f16 v[94:97], v[74:77], v[46:49], 0
	v_mfma_f32_16x16x32_f16 v[46:49], v[98:101], v[46:49], 0
	v_mfma_f32_16x16x32_f16 v[94:97], v[86:89], v[50:53], v[94:97]
	v_mfma_f32_16x16x32_f16 v[50:53], v[106:109], v[50:53], v[46:49]
	v_mfma_f32_16x16x32_f16 v[46:49], v[74:77], v[38:41], 0
	v_mfma_f32_16x16x32_f16 v[38:41], v[98:101], v[38:41], 0
	v_mfma_f32_16x16x32_f16 v[110:113], v[106:109], v[42:45], v[38:41]
	v_mfma_f32_16x16x32_f16 v[38:41], v[74:77], v[30:33], 0
	v_mfma_f32_16x16x32_f16 v[30:33], v[98:101], v[30:33], 0
	v_mfma_f32_16x16x32_f16 v[174:177], v[106:109], v[34:37], v[30:33]
	v_mfma_f32_16x16x32_f16 v[30:33], v[74:77], v[22:25], 0
	v_mfma_f32_16x16x32_f16 v[22:25], v[98:101], v[22:25], 0
	v_mfma_f32_16x16x32_f16 v[102:105], v[86:89], v[42:45], v[46:49]
	v_mfma_f32_16x16x32_f16 v[170:173], v[86:89], v[34:37], v[38:41]
	v_mfma_f32_16x16x32_f16 v[178:181], v[86:89], v[26:29], v[30:33]
	v_mfma_f32_16x16x32_f16 v[182:185], v[106:109], v[26:29], v[22:25]
	s_setprio 0
	s_mov_b32 m0, s58
	s_barrier
	ds_read_b128 v[34:37], v237 offset:16384
	ds_read_b128 v[46:49], v237 offset:17408
	ds_read_b128 v[114:117], v237 offset:18432
	ds_read_b128 v[118:121], v237 offset:19456
	ds_read_b128 v[122:125], v237 offset:20480
	ds_read_b128 v[126:129], v237 offset:21504
	ds_read_b128 v[166:169], v237 offset:22528
	ds_read_b128 v[186:189], v237 offset:23552
	global_load_lds_dwordx4 v220, s[50:51]
	s_mov_b32 m0, s62
	s_nop 0
	global_load_lds_dwordx4 v226, s[50:51]
	s_barrier
	s_waitcnt lgkmcnt(0)
	s_setprio 1
	s_waitcnt lgkmcnt(0)
	v_mfma_f32_16x16x32_f16 v[22:25], v[6:9], v[34:37], 0
	v_mfma_f32_16x16x32_f16 v[30:33], v[6:9], v[114:117], 0
	v_mfma_f32_16x16x32_f16 v[42:45], v[6:9], v[122:125], 0
	v_mfma_f32_16x16x32_f16 v[6:9], v[6:9], v[166:169], 0
	v_mfma_f32_16x16x32_f16 v[22:25], v[10:13], v[46:49], v[22:25]
	v_mfma_f32_16x16x32_f16 v[26:29], v[14:17], v[34:37], 0
	v_mfma_f32_16x16x32_f16 v[30:33], v[10:13], v[118:121], v[30:33]
	v_mfma_f32_16x16x32_f16 v[38:41], v[14:17], v[114:117], 0
	v_mfma_f32_16x16x32_f16 v[42:45], v[10:13], v[126:129], v[42:45]
	v_mfma_f32_16x16x32_f16 v[134:137], v[14:17], v[122:125], 0
	v_mfma_f32_16x16x32_f16 v[6:9], v[10:13], v[186:189], v[6:9]
	v_mfma_f32_16x16x32_f16 v[10:13], v[14:17], v[166:169], 0
	v_mfma_f32_16x16x32_f16 v[26:29], v[18:21], v[46:49], v[26:29]
	v_mfma_f32_16x16x32_f16 v[38:41], v[18:21], v[118:121], v[38:41]
	v_mfma_f32_16x16x32_f16 v[134:137], v[18:21], v[126:129], v[134:137]
	v_mfma_f32_16x16x32_f16 v[14:17], v[18:21], v[186:189], v[10:13]
	s_setprio 0
	s_barrier
	s_add_u32 s86, s48, 0x40000
	s_addc_u32 s87, s49, 0
	s_add_i32 s84, s76, s57
	v_lshl_add_u64 v[10:11], s[86:87], 0, v[216:217]
	s_mov_b32 m0, s84
	s_add_i32 s85, s84, 0x2000
	global_load_lds_dwordx4 v[10:11], off
	v_lshl_add_u64 v[10:11], s[86:87], 0, v[218:219]
	s_mov_b32 m0, s85
	s_nop 0
	global_load_lds_dwordx4 v[10:11], off
	s_add_i32 s94, s61, s33
	s_mov_b32 s95, 0
	s_cmpk_gt_u32 s94, 0x15ff
	s_cselect_b64 s[96:97], -1, 0
	s_and_b64 s[96:97], s[96:97], exec
	s_cselect_b32 s96, 0x7fffea00, 0
	s_cselect_b32 s98, s25, s15
	s_cselect_b32 s99, s24, s14
	s_add_i32 s96, s96, s94
	s_lshl_b32 s94, s96, 1
	s_addk_i32 s94, 0x2c00
	s_lshl_b64 s[96:97], s[94:95], 12
	s_add_u32 s100, s99, s96
	s_addc_u32 s101, s98, s97
	s_add_i32 s94, s75, s61
	s_cmpk_gt_u32 s94, 0x15ff
	s_cselect_b32 s97, 0x7fffea00, 0
	s_cselect_b32 s96, 0x80, 0
	s_add_i32 s97, s97, s94
	s_lshl_b32 s94, s97, 1
	s_add_i32 s97, s94, 0x2c00
	s_mul_hi_u32 s98, s97, 0xba2e8ba3
	s_lshr_b32 s98, s98, 11
	s_mul_i32 s99, s98, 0x7ffff500
	s_add_i32 s99, s99, s97
	s_lshr_b32 s97, s99, 7
	s_mul_i32 s98, s98, 22
	s_add_i32 s97, s97, s98
	s_lshl_b32 s97, s97, 8
	s_and_b32 s94, s94, 0x7e
	s_or_b32 s96, s97, s96
	s_or_b32 s94, s96, s94
	s_lshl_b64 s[96:97], s[94:95], 11
	s_add_i32 s94, s61, -1
	s_cmp_lt_u32 s94, 43
	s_waitcnt vmcnt(6)
	s_cbranch_scc0 .Lhka_rare_a0
	v_cvt_pk_f16_f32 v2, v2, v3
	v_cvt_pk_f16_f32 v3, v4, v5
	v_lshl_add_u64 v[4:5], v[224:225], 0, s[96:97]
	global_store_dwordx2 v[4:5], v[2:3], off
	v_lshlrev_b32_e32 v4, 2, v214
	v_mov_b32_e32 v5, v221
	v_lshl_add_u64 v[4:5], s[100:101], 0, v[4:5]
	global_load_dwordx4 v[2:5], v[4:5], off nt
	s_add_i32 s61, s61, 1

.LBB4_30:
	v_mov_b32_e32 v227, v221
	v_lshl_add_u64 v[54:55], s[50:51], 0, v[220:221]
	v_lshl_add_u64 v[56:57], s[50:51], 0, v[226:227]
	s_add_i32 s50, 0, 0x1c000
	s_mov_b32 m0, s67
	v_add_u32_e32 v238, s50, v234
	v_lshl_add_u64 v[58:59], v[130:131], 0, s[30:31]
	ds_read_b128 v[240:243], v238
	ds_read_b128 v[244:247], v238 offset:1024
	ds_read_b128 v[248:251], v238 offset:2048
	ds_read_b128 v[252:255], v238 offset:3072
	global_load_lds_dwordx4 v[58:59], off
	v_lshl_add_u64 v[58:59], v[132:133], 0, s[30:31]
	s_mov_b32 m0, s68
	s_nop 0
	global_load_lds_dwordx4 v[58:59], off
	s_barrier
	s_waitcnt lgkmcnt(0)
	s_setprio 1
	s_waitcnt lgkmcnt(0)
	v_mfma_f32_16x16x32_f16 v[58:61], v[240:243], v[122:125], v[94:97]
	v_mfma_f32_16x16x32_f16 v[50:53], v[248:251], v[122:125], v[50:53]
	v_mfma_f32_16x16x32_f16 v[130:133], v[244:247], v[126:129], v[58:61]
	v_mfma_f32_16x16x32_f16 v[126:129], v[252:255], v[126:129], v[50:53]
	v_mfma_f32_16x16x32_f16 v[50:53], v[240:243], v[118:121], v[102:105]
	v_mfma_f32_16x16x32_f16 v[122:125], v[244:247], v[210:213], v[50:53]
	v_mfma_f32_16x16x32_f16 v[50:53], v[248:251], v[118:121], v[110:113]
	v_mfma_f32_16x16x32_f16 v[118:121], v[252:255], v[210:213], v[50:53]
	v_mfma_f32_16x16x32_f16 v[50:53], v[240:243], v[202:205], v[170:173]
	v_mfma_f32_16x16x32_f16 v[110:113], v[244:247], v[206:209], v[50:53]
	v_mfma_f32_16x16x32_f16 v[50:53], v[248:251], v[202:205], v[174:177]
	v_mfma_f32_16x16x32_f16 v[102:105], v[252:255], v[206:209], v[50:53]
	v_mfma_f32_16x16x32_f16 v[50:53], v[240:243], v[18:21], v[178:181]
	v_mfma_f32_16x16x32_f16 v[18:21], v[248:251], v[18:21], v[182:185]
	v_mfma_f32_16x16x32_f16 v[94:97], v[244:247], v[198:201], v[50:53]
	v_mfma_f32_16x16x32_f16 v[82:85], v[252:255], v[198:201], v[18:21]
	s_setprio 0
	s_mov_b32 m0, s69
	s_nop 3
	v_lshl_add_u64 v[18:19], v[54:55], 0, s[30:31]
	s_barrier
	ds_read_b128 v[66:69], v237 offset:49152
	ds_read_b128 v[78:81], v237 offset:50176
	ds_read_b128 v[170:173], v237 offset:51200
	ds_read_b128 v[174:177], v237 offset:52224
	ds_read_b128 v[178:181], v237 offset:53248
	ds_read_b128 v[182:185], v237 offset:54272
	ds_read_b128 v[198:201], v237 offset:55296
	ds_read_b128 v[202:205], v237 offset:56320
	global_load_lds_dwordx4 v[18:19], off
	v_lshl_add_u64 v[18:19], v[56:57], 0, s[30:31]
	s_mov_b32 m0, s70
	s_nop 0
	global_load_lds_dwordx4 v[18:19], off
	s_barrier
	s_waitcnt lgkmcnt(0)
	s_setprio 1
	s_waitcnt lgkmcnt(0)
	v_mfma_f32_16x16x32_f16 v[18:21], v[10:13], v[66:69], v[22:25]
	v_mfma_f32_16x16x32_f16 v[70:73], v[186:189], v[78:81], v[18:21]
	v_mfma_f32_16x16x32_f16 v[18:21], v[190:193], v[66:69], v[26:29]
	v_mfma_f32_16x16x32_f16 v[58:61], v[194:197], v[78:81], v[18:21]
	v_mfma_f32_16x16x32_f16 v[18:21], v[10:13], v[170:173], v[30:33]
	v_mfma_f32_16x16x32_f16 v[50:53], v[186:189], v[174:177], v[18:21]
	v_mfma_f32_16x16x32_f16 v[18:21], v[190:193], v[170:173], v[38:41]
	v_mfma_f32_16x16x32_f16 v[38:41], v[194:197], v[174:177], v[18:21]
	v_mfma_f32_16x16x32_f16 v[18:21], v[10:13], v[178:181], v[42:45]
	v_mfma_f32_16x16x32_f16 v[6:9], v[10:13], v[198:201], v[6:9]
	v_mfma_f32_16x16x32_f16 v[26:29], v[186:189], v[182:185], v[18:21]
	v_mfma_f32_16x16x32_f16 v[18:21], v[190:193], v[178:181], v[134:137]
	v_mfma_f32_16x16x32_f16 v[10:13], v[186:189], v[202:205], v[6:9]
	v_mfma_f32_16x16x32_f16 v[6:9], v[190:193], v[198:201], v[14:17]
	v_mfma_f32_16x16x32_f16 v[18:21], v[194:197], v[182:185], v[18:21]
	v_mfma_f32_16x16x32_f16 v[6:9], v[194:197], v[202:205], v[6:9]
	s_setprio 0
	s_barrier
	s_add_u32 s48, s48, 0x40080
	s_addc_u32 s49, s49, 0
	s_add_i32 s50, s50, s57
	v_lshl_add_u64 v[14:15], s[48:49], 0, v[216:217]
	s_mov_b32 m0, s50
	s_add_i32 s51, s50, 0x2000
	global_load_lds_dwordx4 v[14:15], off
	v_lshl_add_u64 v[14:15], s[48:49], 0, v[218:219]
	s_mov_b32 m0, s51
	s_nop 0
	global_load_lds_dwordx4 v[14:15], off
	s_add_i32 s94, s61, s33
	s_mov_b32 s95, 0
	s_cmpk_gt_u32 s94, 0x15ff
	s_cselect_b64 s[96:97], -1, 0
	s_and_b64 s[96:97], s[96:97], exec
	s_cselect_b32 s96, 0x7fffea00, 0
	s_cselect_b32 s98, s25, s15
	s_cselect_b32 s99, s24, s14
	s_add_i32 s96, s96, s94
	s_lshl_b32 s94, s96, 1
	s_addk_i32 s94, 0x2c00
	s_lshl_b64 s[96:97], s[94:95], 12
	s_add_u32 s100, s99, s96
	s_addc_u32 s101, s98, s97
	s_add_i32 s94, s75, s61
	s_cmpk_gt_u32 s94, 0x15ff
	s_cselect_b32 s97, 0x7fffea00, 0
	s_cselect_b32 s96, 0x80, 0
	s_add_i32 s97, s97, s94
	s_lshl_b32 s94, s97, 1
	s_add_i32 s97, s94, 0x2c00
	s_mul_hi_u32 s98, s97, 0xba2e8ba3
	s_lshr_b32 s98, s98, 11
	s_mul_i32 s99, s98, 0x7ffff500
	s_add_i32 s99, s99, s97
	s_lshr_b32 s97, s99, 7
	s_mul_i32 s98, s98, 22
	s_add_i32 s97, s97, s98
	s_lshl_b32 s97, s97, 8
	s_and_b32 s94, s94, 0x7e
	s_or_b32 s96, s97, s96
	s_or_b32 s94, s96, s94
	s_lshl_b64 s[96:97], s[94:95], 11
	s_add_i32 s94, s61, -1
	s_cmp_lt_u32 s94, 43
	s_waitcnt vmcnt(6)
	s_cbranch_scc0 .Lhka_rare_a1
	v_cvt_pk_f16_f32 v2, v2, v3
	v_cvt_pk_f16_f32 v3, v4, v5
	v_lshl_add_u64 v[4:5], v[224:225], 0, s[96:97]
	global_store_dwordx2 v[4:5], v[2:3], off
	v_lshlrev_b32_e32 v4, 2, v214
	v_mov_b32_e32 v5, v221
	v_lshl_add_u64 v[4:5], s[100:101], 0, v[4:5]
	global_load_dwordx4 v[2:5], v[4:5], off nt
	s_add_i32 s61, s61, 1

.LBB4_40:
	s_add_u32 s28, s46, 0x80
	s_addc_u32 s48, s47, 0
	s_and_b64 s[44:45], s[44:45], exec
	s_cselect_b32 s45, s54, s87
	s_cselect_b32 s44, s55, s86
	s_mov_b32 m0, s59
	v_lshl_add_u64 v[182:183], s[44:45], 0, v[216:217]
	ds_read_b128 v[186:189], v229
	ds_read_b128 v[190:193], v229 offset:1024
	ds_read_b128 v[194:197], v229 offset:2048
	ds_read_b128 v[198:201], v229 offset:3072
	global_load_lds_dwordx4 v[182:183], off
	v_lshl_add_u64 v[184:185], s[44:45], 0, v[218:219]
	s_mov_b32 m0, s60
	s_cselect_b32 s49, s52, s48
	global_load_lds_dwordx4 v[184:185], off
	s_barrier
	s_waitcnt lgkmcnt(0)
	s_cselect_b32 s48, s53, s28
	s_setprio 1
	s_waitcnt lgkmcnt(0)
	v_mfma_f32_16x16x32_f16 v[130:133], v[186:189], v[174:177], v[130:133]
	v_mfma_f32_16x16x32_f16 v[126:129], v[194:197], v[174:177], v[126:129]
	v_mfma_f32_16x16x32_f16 v[122:125], v[186:189], v[166:169], v[122:125]
	v_mfma_f32_16x16x32_f16 v[118:121], v[194:197], v[166:169], v[118:121]
	v_mfma_f32_16x16x32_f16 v[110:113], v[186:189], v[158:161], v[110:113]
	v_mfma_f32_16x16x32_f16 v[102:105], v[194:197], v[158:161], v[102:105]
	v_mfma_f32_16x16x32_f16 v[94:97], v[186:189], v[150:153], v[94:97]
	v_mfma_f32_16x16x32_f16 v[82:85], v[194:197], v[150:153], v[82:85]
	v_mfma_f32_16x16x32_f16 v[130:133], v[190:193], v[178:181], v[130:133]
	v_mfma_f32_16x16x32_f16 v[126:129], v[198:201], v[178:181], v[126:129]
	v_mfma_f32_16x16x32_f16 v[122:125], v[190:193], v[170:173], v[122:125]
	v_mfma_f32_16x16x32_f16 v[118:121], v[198:201], v[170:173], v[118:121]
	v_mfma_f32_16x16x32_f16 v[110:113], v[190:193], v[162:165], v[110:113]
	v_mfma_f32_16x16x32_f16 v[102:105], v[198:201], v[162:165], v[102:105]
	v_mfma_f32_16x16x32_f16 v[94:97], v[190:193], v[154:157], v[94:97]
	v_mfma_f32_16x16x32_f16 v[82:85], v[198:201], v[154:157], v[82:85]
	s_setprio 0
	s_mov_b32 m0, s58
	s_barrier
	ds_read_b128 v[150:153], v237 offset:16384
	ds_read_b128 v[154:157], v237 offset:17408
	ds_read_b128 v[158:161], v237 offset:18432
	ds_read_b128 v[162:165], v237 offset:19456
	ds_read_b128 v[166:169], v237 offset:20480
	ds_read_b128 v[170:173], v237 offset:21504
	ds_read_b128 v[174:177], v237 offset:22528
	ds_read_b128 v[178:181], v237 offset:23552
	global_load_lds_dwordx4 v220, s[48:49]
	s_mov_b32 m0, s62
	s_nop 0
	global_load_lds_dwordx4 v226, s[48:49]
	s_barrier
	s_waitcnt lgkmcnt(0)
	s_setprio 1
	s_waitcnt lgkmcnt(0)
	v_mfma_f32_16x16x32_f16 v[70:73], v[134:137], v[150:153], v[70:73]
	v_mfma_f32_16x16x32_f16 v[58:61], v[142:145], v[150:153], v[58:61]
	v_mfma_f32_16x16x32_f16 v[50:53], v[134:137], v[158:161], v[50:53]
	v_mfma_f32_16x16x32_f16 v[38:41], v[142:145], v[158:161], v[38:41]
	v_mfma_f32_16x16x32_f16 v[26:29], v[134:137], v[166:169], v[26:29]
	v_mfma_f32_16x16x32_f16 v[18:21], v[142:145], v[166:169], v[18:21]
	v_mfma_f32_16x16x32_f16 v[10:13], v[134:137], v[174:177], v[10:13]
	v_mfma_f32_16x16x32_f16 v[6:9], v[142:145], v[174:177], v[6:9]
	v_mfma_f32_16x16x32_f16 v[70:73], v[138:141], v[154:157], v[70:73]
	v_mfma_f32_16x16x32_f16 v[58:61], v[146:149], v[154:157], v[58:61]
	v_mfma_f32_16x16x32_f16 v[50:53], v[138:141], v[162:165], v[50:53]
	v_mfma_f32_16x16x32_f16 v[38:41], v[146:149], v[162:165], v[38:41]
	v_mfma_f32_16x16x32_f16 v[26:29], v[138:141], v[170:173], v[26:29]
	v_mfma_f32_16x16x32_f16 v[18:21], v[146:149], v[170:173], v[18:21]
	v_mfma_f32_16x16x32_f16 v[10:13], v[138:141], v[178:181], v[10:13]
	v_mfma_f32_16x16x32_f16 v[6:9], v[146:149], v[178:181], v[6:9]
	s_setprio 0
	s_barrier
	s_add_u32 s90, s44, 0x40000
	s_addc_u32 s91, s45, 0
	s_mov_b32 m0, s84
	v_lshl_add_u64 v[134:135], s[90:91], 0, v[216:217]
	global_load_lds_dwordx4 v[134:135], off
	v_lshl_add_u64 v[134:135], s[90:91], 0, v[218:219]
	s_mov_b32 m0, s85
	s_nop 0
	global_load_lds_dwordx4 v[134:135], off
	s_add_i32 s94, s61, s33
	s_mov_b32 s95, 0
	s_cmpk_gt_u32 s94, 0x15ff
	s_cselect_b64 s[96:97], -1, 0
	s_and_b64 s[96:97], s[96:97], exec
	s_cselect_b32 s96, 0x7fffea00, 0
	s_cselect_b32 s98, s25, s15
	s_cselect_b32 s99, s24, s14
	s_add_i32 s96, s96, s94
	s_lshl_b32 s94, s96, 1
	s_addk_i32 s94, 0x2c00
	s_lshl_b64 s[96:97], s[94:95], 12
	s_add_u32 s100, s99, s96
	s_addc_u32 s101, s98, s97
	s_add_i32 s94, s75, s61
	s_cmpk_gt_u32 s94, 0x15ff
	s_cselect_b32 s97, 0x7fffea00, 0
	s_cselect_b32 s96, 0x80, 0
	s_add_i32 s97, s97, s94
	s_lshl_b32 s94, s97, 1
	s_add_i32 s97, s94, 0x2c00
	s_mul_hi_u32 s98, s97, 0xba2e8ba3
	s_lshr_b32 s98, s98, 11
	s_mul_i32 s99, s98, 0x7ffff500
	s_add_i32 s99, s99, s97
	s_lshr_b32 s97, s99, 7
	s_mul_i32 s98, s98, 22
	s_add_i32 s97, s97, s98
	s_lshl_b32 s97, s97, 8
	s_and_b32 s94, s94, 0x7e
	s_or_b32 s96, s97, s96
	s_or_b32 s94, s96, s94
	s_lshl_b64 s[96:97], s[94:95], 11
	s_add_i32 s94, s61, -1
	s_cmp_lt_u32 s94, 43
	s_waitcnt vmcnt(6)
	s_cbranch_scc0 .Lhka_rare_a2
	v_cvt_pk_f16_f32 v2, v2, v3
	v_cvt_pk_f16_f32 v3, v4, v5
	v_lshl_add_u64 v[4:5], v[224:225], 0, s[96:97]
	global_store_dwordx2 v[4:5], v[2:3], off
	v_lshlrev_b32_e32 v4, 2, v214
	v_mov_b32_e32 v5, v221
	v_lshl_add_u64 v[4:5], s[100:101], 0, v[4:5]
	global_load_dwordx4 v[2:5], v[4:5], off nt
	s_add_i32 s61, s61, 1

.LBB4_46:
	s_mov_b32 m0, s67
	v_lshl_add_u64 v[182:183], v[182:183], 0, s[30:31]
	ds_read_b128 v[190:193], v238
	ds_read_b128 v[194:197], v238 offset:1024
	ds_read_b128 v[198:201], v238 offset:2048
	ds_read_b128 v[202:205], v238 offset:3072
	global_load_lds_dwordx4 v[182:183], off
	v_lshl_add_u64 v[182:183], v[184:185], 0, s[30:31]
	s_mov_b32 m0, s68
	v_mov_b32_e32 v227, v221
	global_load_lds_dwordx4 v[182:183], off
	s_barrier
	s_waitcnt lgkmcnt(0)
	v_lshl_add_u64 v[186:187], s[48:49], 0, v[220:221]
	v_lshl_add_u64 v[188:189], s[48:49], 0, v[226:227]
	s_setprio 1
	s_waitcnt lgkmcnt(0)
	v_mfma_f32_16x16x32_f16 v[130:133], v[190:193], v[174:177], v[130:133]
	v_mfma_f32_16x16x32_f16 v[126:129], v[198:201], v[174:177], v[126:129]
	v_mfma_f32_16x16x32_f16 v[122:125], v[190:193], v[166:169], v[122:125]
	v_mfma_f32_16x16x32_f16 v[118:121], v[198:201], v[166:169], v[118:121]
	v_mfma_f32_16x16x32_f16 v[110:113], v[190:193], v[158:161], v[110:113]
	v_mfma_f32_16x16x32_f16 v[102:105], v[198:201], v[158:161], v[102:105]
	v_mfma_f32_16x16x32_f16 v[94:97], v[190:193], v[150:153], v[94:97]
	v_mfma_f32_16x16x32_f16 v[82:85], v[198:201], v[150:153], v[82:85]
	v_mfma_f32_16x16x32_f16 v[130:133], v[194:197], v[178:181], v[130:133]
	v_mfma_f32_16x16x32_f16 v[126:129], v[202:205], v[178:181], v[126:129]
	v_mfma_f32_16x16x32_f16 v[122:125], v[194:197], v[170:173], v[122:125]
	v_mfma_f32_16x16x32_f16 v[118:121], v[202:205], v[170:173], v[118:121]
	v_mfma_f32_16x16x32_f16 v[110:113], v[194:197], v[162:165], v[110:113]
	v_mfma_f32_16x16x32_f16 v[102:105], v[202:205], v[162:165], v[102:105]
	v_mfma_f32_16x16x32_f16 v[94:97], v[194:197], v[154:157], v[94:97]
	v_mfma_f32_16x16x32_f16 v[82:85], v[202:205], v[154:157], v[82:85]
	s_setprio 0
	s_mov_b32 m0, s69
	v_lshl_add_u64 v[182:183], v[186:187], 0, s[30:31]
	s_barrier
	ds_read_b128 v[150:153], v237 offset:49152
	ds_read_b128 v[154:157], v237 offset:50176
	ds_read_b128 v[158:161], v237 offset:51200
	ds_read_b128 v[162:165], v237 offset:52224
	ds_read_b128 v[166:169], v237 offset:53248
	ds_read_b128 v[170:173], v237 offset:54272
	ds_read_b128 v[174:177], v237 offset:55296
	ds_read_b128 v[178:181], v237 offset:56320
	global_load_lds_dwordx4 v[182:183], off
	v_lshl_add_u64 v[182:183], v[188:189], 0, s[30:31]
	s_mov_b32 m0, s70
	s_nop 0
	global_load_lds_dwordx4 v[182:183], off
	s_barrier
	s_waitcnt lgkmcnt(0)
	s_setprio 1
	s_waitcnt lgkmcnt(0)
	v_mfma_f32_16x16x32_f16 v[70:73], v[134:137], v[150:153], v[70:73]
	v_mfma_f32_16x16x32_f16 v[58:61], v[142:145], v[150:153], v[58:61]
	v_mfma_f32_16x16x32_f16 v[50:53], v[134:137], v[158:161], v[50:53]
	v_mfma_f32_16x16x32_f16 v[38:41], v[142:145], v[158:161], v[38:41]
	v_mfma_f32_16x16x32_f16 v[26:29], v[134:137], v[166:169], v[26:29]
	v_mfma_f32_16x16x32_f16 v[18:21], v[142:145], v[166:169], v[18:21]
	v_mfma_f32_16x16x32_f16 v[10:13], v[134:137], v[174:177], v[10:13]
	v_mfma_f32_16x16x32_f16 v[6:9], v[142:145], v[174:177], v[6:9]
	v_mfma_f32_16x16x32_f16 v[70:73], v[138:141], v[154:157], v[70:73]
	v_mfma_f32_16x16x32_f16 v[58:61], v[146:149], v[154:157], v[58:61]
	v_mfma_f32_16x16x32_f16 v[50:53], v[138:141], v[162:165], v[50:53]
	v_mfma_f32_16x16x32_f16 v[38:41], v[146:149], v[162:165], v[38:41]
	v_mfma_f32_16x16x32_f16 v[26:29], v[138:141], v[170:173], v[26:29]
	v_mfma_f32_16x16x32_f16 v[18:21], v[146:149], v[170:173], v[18:21]
	v_mfma_f32_16x16x32_f16 v[10:13], v[138:141], v[178:181], v[10:13]
	v_mfma_f32_16x16x32_f16 v[6:9], v[146:149], v[178:181], v[6:9]
	s_setprio 0
	s_barrier
	s_add_u32 s44, s44, 0x40080
	s_addc_u32 s45, s45, 0
	s_mov_b32 m0, s50
	v_lshl_add_u64 v[134:135], s[44:45], 0, v[216:217]
	global_load_lds_dwordx4 v[134:135], off
	v_lshl_add_u64 v[134:135], s[44:45], 0, v[218:219]
	s_mov_b32 m0, s51
	s_nop 0
	global_load_lds_dwordx4 v[134:135], off
	s_add_i32 s94, s61, s33
	s_mov_b32 s95, 0
	s_cmpk_gt_u32 s94, 0x15ff
	s_cselect_b64 s[96:97], -1, 0
	s_and_b64 s[96:97], s[96:97], exec
	s_cselect_b32 s96, 0x7fffea00, 0
	s_cselect_b32 s98, s25, s15
	s_cselect_b32 s99, s24, s14
	s_add_i32 s96, s96, s94
	s_lshl_b32 s94, s96, 1
	s_addk_i32 s94, 0x2c00
	s_lshl_b64 s[96:97], s[94:95], 12
	s_add_u32 s100, s99, s96
	s_addc_u32 s101, s98, s97
	s_add_i32 s94, s75, s61
	s_cmpk_gt_u32 s94, 0x15ff
	s_cselect_b32 s97, 0x7fffea00, 0
	s_cselect_b32 s96, 0x80, 0
	s_add_i32 s97, s97, s94
	s_lshl_b32 s94, s97, 1
	s_add_i32 s97, s94, 0x2c00
	s_mul_hi_u32 s98, s97, 0xba2e8ba3
	s_lshr_b32 s98, s98, 11
	s_mul_i32 s99, s98, 0x7ffff500
	s_add_i32 s99, s99, s97
	s_lshr_b32 s97, s99, 7
	s_mul_i32 s98, s98, 22
	s_add_i32 s97, s97, s98
	s_lshl_b32 s97, s97, 8
	s_and_b32 s94, s94, 0x7e
	s_or_b32 s96, s97, s96
	s_or_b32 s94, s96, s94
	s_lshl_b64 s[96:97], s[94:95], 11
	s_add_i32 s28, s88, 2
	s_add_u32 s46, s46, 0x100
	s_addc_u32 s47, s47, 0
	s_add_u32 s86, s86, 0x100
	s_addc_u32 s87, s87, 0
	s_add_i32 s94, s61, -1
	s_cmp_lt_u32 s94, 43
	s_waitcnt vmcnt(6)
	s_cbranch_scc0 .Lhka_rare_a3
	v_cvt_pk_f16_f32 v2, v2, v3
	v_cvt_pk_f16_f32 v3, v4, v5
	v_lshl_add_u64 v[4:5], v[224:225], 0, s[96:97]
	global_store_dwordx2 v[4:5], v[2:3], off
	v_lshlrev_b32_e32 v4, 2, v214
	v_mov_b32_e32 v5, v221
	v_lshl_add_u64 v[4:5], s[100:101], 0, v[4:5]
	global_load_dwordx4 v[2:5], v[4:5], off nt
	s_add_i32 s61, s61, 1

.Lhka_rare_a0:
	s_cmp_gt_i32 s61, 44
	s_cbranch_scc1 .Lhka_done_a0
	s_cmp_lt_i32 s61, 1
	s_cbranch_scc1 .Lhka_rld_a0
	v_cvt_pk_f16_f32 v2, v2, v3
	v_cvt_pk_f16_f32 v3, v4, v5
	v_lshl_add_u64 v[4:5], v[224:225], 0, s[96:97]
	global_store_dwordx2 v[4:5], v[2:3], off

.Lhka_rinc_a0:
	s_add_i32 s61, s61, 1
	s_branch .Lhka_done_a0

.Lhka_rinc_a3:
	s_add_i32 s61, s61, 1
	s_branch .Lhka_done_a3
	.p2align	8

.LBB5_18:
.LBB5_24:
	s_and_b64 s[46:47], s[38:39], exec
	s_cselect_b32 s48, s35, s43
	s_cselect_b32 s49, s34, s42
	s_cselect_b32 s50, s37, s41
	s_cselect_b32 s51, s36, s40
	s_add_u32 s24, s42, 0x100
	s_addc_u32 s80, s43, 0
	s_and_b64 s[46:47], s[44:45], exec
	s_cselect_b32 s47, s48, s80
	s_cselect_b32 s46, s49, s24
	s_add_u32 s24, s40, 0x100
	s_addc_u32 s80, s41, 0
	s_and_b64 s[44:45], s[44:45], exec
	s_cselect_b32 s45, s50, s80
	s_cselect_b32 s44, s51, s24
	s_mov_b32 m0, s55
	v_add_u32_e32 v227, s72, v232
	v_lshl_add_u64 v[130:131], s[44:45], 0, v[212:213]
	ds_read_b128 v[82:85], v227
	ds_read_b128 v[94:97], v227 offset:1024
	ds_read_b128 v[102:105], v227 offset:2048
	ds_read_b128 v[110:113], v227 offset:3072
	global_load_lds_dwordx4 v[130:131], off
	v_lshl_add_u64 v[132:133], s[44:45], 0, v[214:215]
	s_mov_b32 m0, s56
	s_nop 0
	global_load_lds_dwordx4 v[132:133], off
	s_barrier
	s_waitcnt lgkmcnt(0)
	s_setprio 1
	s_waitcnt lgkmcnt(0)
	v_mfma_f32_16x16x32_f16 v[90:93], v[82:85], v[46:49], 0
	v_mfma_f32_16x16x32_f16 v[46:49], v[102:105], v[46:49], 0
	v_mfma_f32_16x16x32_f16 v[90:93], v[94:97], v[50:53], v[90:93]
	v_mfma_f32_16x16x32_f16 v[46:49], v[110:113], v[50:53], v[46:49]
	v_mfma_f32_16x16x32_f16 v[50:53], v[82:85], v[38:41], 0
	v_mfma_f32_16x16x32_f16 v[38:41], v[102:105], v[38:41], 0
	v_mfma_f32_16x16x32_f16 v[106:109], v[110:113], v[42:45], v[38:41]
	v_mfma_f32_16x16x32_f16 v[38:41], v[82:85], v[30:33], 0
	v_mfma_f32_16x16x32_f16 v[30:33], v[102:105], v[30:33], 0
	v_mfma_f32_16x16x32_f16 v[170:173], v[110:113], v[34:37], v[30:33]
	v_mfma_f32_16x16x32_f16 v[30:33], v[82:85], v[22:25], 0
	v_mfma_f32_16x16x32_f16 v[22:25], v[102:105], v[22:25], 0
	v_mfma_f32_16x16x32_f16 v[98:101], v[94:97], v[42:45], v[50:53]
	v_mfma_f32_16x16x32_f16 v[166:169], v[94:97], v[34:37], v[38:41]
	v_mfma_f32_16x16x32_f16 v[174:177], v[94:97], v[26:29], v[30:33]
	v_mfma_f32_16x16x32_f16 v[178:181], v[110:113], v[26:29], v[22:25]
	s_setprio 0
	s_mov_b32 m0, s54
	s_barrier
	ds_read_b128 v[42:45], v235 offset:16384
	ds_read_b128 v[114:117], v235 offset:17408
	ds_read_b128 v[118:121], v235 offset:18432
	ds_read_b128 v[122:125], v235 offset:19456
	ds_read_b128 v[126:129], v235 offset:20480
	ds_read_b128 v[154:157], v235 offset:21504
	ds_read_b128 v[162:165], v235 offset:22528
	ds_read_b128 v[182:185], v235 offset:23552
	global_load_lds_dwordx4 v216, s[46:47]
	s_mov_b32 m0, s57
	s_nop 0
	global_load_lds_dwordx4 v222, s[46:47]
	s_barrier
	s_waitcnt lgkmcnt(0)
	s_setprio 1
	s_waitcnt lgkmcnt(0)
	v_mfma_f32_16x16x32_f16 v[22:25], v[6:9], v[42:45], 0
	v_mfma_f32_16x16x32_f16 v[30:33], v[6:9], v[118:121], 0
	v_mfma_f32_16x16x32_f16 v[38:41], v[6:9], v[126:129], 0
	v_mfma_f32_16x16x32_f16 v[6:9], v[6:9], v[162:165], 0
	v_mfma_f32_16x16x32_f16 v[22:25], v[10:13], v[114:117], v[22:25]
	v_mfma_f32_16x16x32_f16 v[26:29], v[14:17], v[42:45], 0
	v_mfma_f32_16x16x32_f16 v[30:33], v[10:13], v[122:125], v[30:33]
	v_mfma_f32_16x16x32_f16 v[34:37], v[14:17], v[118:121], 0
	v_mfma_f32_16x16x32_f16 v[38:41], v[10:13], v[154:157], v[38:41]
	v_mfma_f32_16x16x32_f16 v[50:53], v[14:17], v[126:129], 0
	v_mfma_f32_16x16x32_f16 v[6:9], v[10:13], v[182:185], v[6:9]
	v_mfma_f32_16x16x32_f16 v[10:13], v[14:17], v[162:165], 0
	v_mfma_f32_16x16x32_f16 v[26:29], v[18:21], v[114:117], v[26:29]
	v_mfma_f32_16x16x32_f16 v[34:37], v[18:21], v[122:125], v[34:37]
	v_mfma_f32_16x16x32_f16 v[50:53], v[18:21], v[154:157], v[50:53]
	v_mfma_f32_16x16x32_f16 v[14:17], v[18:21], v[182:185], v[10:13]
	s_setprio 0
	s_barrier
	s_add_u32 s82, s44, 0x40000
	s_addc_u32 s83, s45, 0
	s_add_i32 s80, s72, s53
	v_lshl_add_u64 v[10:11], s[82:83], 0, v[212:213]
	s_mov_b32 m0, s80
	s_add_i32 s81, s80, 0x2000
	global_load_lds_dwordx4 v[10:11], off
	v_lshl_add_u64 v[10:11], s[82:83], 0, v[214:215]
	s_mov_b32 m0, s81
	s_nop 0
	global_load_lds_dwordx4 v[10:11], off
	s_add_i32 s92, s71, s63
	s_mov_b32 s93, 0
	s_lshl_b64 s[90:91], s[92:93], 12
	s_add_i32 s92, s63, s33
	s_lshl_b64 s[92:93], s[92:93], 13
	s_add_i32 s94, s63, -1
	s_cmp_lt_u32 s94, 43
	s_waitcnt vmcnt(6)
	s_cbranch_scc0 .Lhkb_rare_b0
	v_cvt_pk_f16_f32 v2, v2, v3
	v_cvt_pk_f16_f32 v3, v4, v5
	v_lshl_add_u64 v[4:5], v[220:221], 0, s[90:91]
	global_store_dwordx2 v[4:5], v[2:3], off
	v_lshl_add_u64 v[4:5], v[224:225], 0, s[92:93]
	global_load_dwordx4 v[2:5], v[4:5], off nt
	s_add_i32 s63, s63, 1

.LBB5_30:
	v_mov_b32_e32 v223, v217
	v_lshl_add_u64 v[58:59], s[46:47], 0, v[216:217]
	v_lshl_add_u64 v[60:61], s[46:47], 0, v[222:223]
	s_add_i32 s46, 0, 0x1c000
	s_mov_b32 m0, s62
	v_add_u32_e32 v236, s46, v232
	v_lshl_add_u64 v[62:63], v[130:131], 0, s[26:27]
	ds_read_b128 v[238:241], v236
	ds_read_b128 v[242:245], v236 offset:1024
	ds_read_b128 v[246:249], v236 offset:2048
	ds_read_b128 v[250:253], v236 offset:3072
	global_load_lds_dwordx4 v[62:63], off
	v_lshl_add_u64 v[62:63], v[132:133], 0, s[26:27]
	s_mov_b32 m0, s64
	s_nop 0
	global_load_lds_dwordx4 v[62:63], off
	s_barrier
	s_waitcnt lgkmcnt(0)
	s_setprio 1
	s_waitcnt lgkmcnt(0)
	v_mfma_f32_16x16x32_f16 v[62:65], v[238:241], v[122:125], v[90:93]
	v_mfma_f32_16x16x32_f16 v[46:49], v[246:249], v[122:125], v[46:49]
	v_mfma_f32_16x16x32_f16 v[130:133], v[242:245], v[126:129], v[62:65]
	v_mfma_f32_16x16x32_f16 v[126:129], v[250:253], v[126:129], v[46:49]
	v_mfma_f32_16x16x32_f16 v[46:49], v[238:241], v[114:117], v[98:101]
	v_mfma_f32_16x16x32_f16 v[122:125], v[242:245], v[206:209], v[46:49]
	v_mfma_f32_16x16x32_f16 v[46:49], v[246:249], v[114:117], v[106:109]
	v_mfma_f32_16x16x32_f16 v[114:117], v[250:253], v[206:209], v[46:49]
	v_mfma_f32_16x16x32_f16 v[46:49], v[238:241], v[198:201], v[166:169]
	v_mfma_f32_16x16x32_f16 v[106:109], v[242:245], v[202:205], v[46:49]
	v_mfma_f32_16x16x32_f16 v[46:49], v[246:249], v[198:201], v[170:173]
	v_mfma_f32_16x16x32_f16 v[98:101], v[250:253], v[202:205], v[46:49]
	v_mfma_f32_16x16x32_f16 v[46:49], v[238:241], v[18:21], v[174:177]
	v_mfma_f32_16x16x32_f16 v[18:21], v[246:249], v[18:21], v[178:181]
	v_mfma_f32_16x16x32_f16 v[90:93], v[242:245], v[194:197], v[46:49]
	v_mfma_f32_16x16x32_f16 v[78:81], v[250:253], v[194:197], v[18:21]
	s_setprio 0
	s_mov_b32 m0, s65
	s_nop 3
	v_lshl_add_u64 v[18:19], v[58:59], 0, s[26:27]
	s_barrier
	ds_read_b128 v[62:65], v235 offset:49152
	ds_read_b128 v[74:77], v235 offset:50176
	ds_read_b128 v[166:169], v235 offset:51200
	ds_read_b128 v[170:173], v235 offset:52224
	ds_read_b128 v[174:177], v235 offset:53248
	ds_read_b128 v[178:181], v235 offset:54272
	ds_read_b128 v[194:197], v235 offset:55296
	ds_read_b128 v[198:201], v235 offset:56320
	global_load_lds_dwordx4 v[18:19], off
	v_lshl_add_u64 v[18:19], v[60:61], 0, s[26:27]
	s_mov_b32 m0, s66
	s_nop 0
	global_load_lds_dwordx4 v[18:19], off
	s_barrier
	s_waitcnt lgkmcnt(0)
	s_setprio 1
	s_waitcnt lgkmcnt(0)
	v_mfma_f32_16x16x32_f16 v[18:21], v[10:13], v[62:65], v[22:25]
	v_mfma_f32_16x16x32_f16 v[70:73], v[182:185], v[74:77], v[18:21]
	v_mfma_f32_16x16x32_f16 v[18:21], v[186:189], v[62:65], v[26:29]
	v_mfma_f32_16x16x32_f16 v[58:61], v[190:193], v[74:77], v[18:21]
	v_mfma_f32_16x16x32_f16 v[18:21], v[10:13], v[166:169], v[30:33]
	v_mfma_f32_16x16x32_f16 v[46:49], v[182:185], v[170:173], v[18:21]
	v_mfma_f32_16x16x32_f16 v[18:21], v[186:189], v[166:169], v[34:37]
	v_mfma_f32_16x16x32_f16 v[34:37], v[190:193], v[170:173], v[18:21]
	v_mfma_f32_16x16x32_f16 v[18:21], v[10:13], v[174:177], v[38:41]
	v_mfma_f32_16x16x32_f16 v[6:9], v[10:13], v[194:197], v[6:9]
	v_mfma_f32_16x16x32_f16 v[26:29], v[182:185], v[178:181], v[18:21]
	v_mfma_f32_16x16x32_f16 v[18:21], v[186:189], v[174:177], v[50:53]
	v_mfma_f32_16x16x32_f16 v[10:13], v[182:185], v[198:201], v[6:9]
	v_mfma_f32_16x16x32_f16 v[6:9], v[186:189], v[194:197], v[14:17]
	v_mfma_f32_16x16x32_f16 v[18:21], v[190:193], v[178:181], v[18:21]
	v_mfma_f32_16x16x32_f16 v[6:9], v[190:193], v[198:201], v[6:9]
	s_setprio 0
	s_barrier
	s_add_u32 s44, s44, 0x40080
	s_addc_u32 s45, s45, 0
	s_add_i32 s46, s46, s53
	v_lshl_add_u64 v[14:15], s[44:45], 0, v[212:213]
	s_mov_b32 m0, s46
	s_add_i32 s47, s46, 0x2000
	global_load_lds_dwordx4 v[14:15], off
	v_lshl_add_u64 v[14:15], s[44:45], 0, v[214:215]
	s_mov_b32 m0, s47
	s_nop 0
	global_load_lds_dwordx4 v[14:15], off
	s_add_i32 s92, s71, s63
	s_mov_b32 s93, 0
	s_lshl_b64 s[90:91], s[92:93], 12
	s_add_i32 s92, s63, s33
	s_lshl_b64 s[92:93], s[92:93], 13
	s_add_i32 s94, s63, -1
	s_cmp_lt_u32 s94, 43
	s_waitcnt vmcnt(6)
	s_cbranch_scc0 .Lhkb_rare_b1
	v_cvt_pk_f16_f32 v2, v2, v3
	v_cvt_pk_f16_f32 v3, v4, v5
	v_lshl_add_u64 v[4:5], v[220:221], 0, s[90:91]
	global_store_dwordx2 v[4:5], v[2:3], off
	v_lshl_add_u64 v[4:5], v[224:225], 0, s[92:93]
	global_load_dwordx4 v[2:5], v[4:5], off nt
	s_add_i32 s63, s63, 1

.LBB5_40:
	s_add_u32 s24, s42, 0x80
	s_addc_u32 s44, s43, 0
	s_and_b64 s[40:41], s[40:41], exec
	s_cselect_b32 s41, s50, s83
	s_cselect_b32 s40, s51, s82
	s_mov_b32 m0, s55
	v_lshl_add_u64 v[182:183], s[40:41], 0, v[212:213]
	ds_read_b128 v[186:189], v227
	ds_read_b128 v[190:193], v227 offset:1024
	ds_read_b128 v[194:197], v227 offset:2048
	ds_read_b128 v[198:201], v227 offset:3072
	global_load_lds_dwordx4 v[182:183], off
	v_lshl_add_u64 v[184:185], s[40:41], 0, v[214:215]
	s_mov_b32 m0, s56
	s_cselect_b32 s45, s48, s44
	global_load_lds_dwordx4 v[184:185], off
	s_barrier
	s_waitcnt lgkmcnt(0)
	s_cselect_b32 s44, s49, s24
	s_setprio 1
	s_waitcnt lgkmcnt(0)
	v_mfma_f32_16x16x32_f16 v[130:133], v[186:189], v[174:177], v[130:133]
	v_mfma_f32_16x16x32_f16 v[126:129], v[194:197], v[174:177], v[126:129]
	v_mfma_f32_16x16x32_f16 v[122:125], v[186:189], v[166:169], v[122:125]
	v_mfma_f32_16x16x32_f16 v[114:117], v[194:197], v[166:169], v[114:117]
	v_mfma_f32_16x16x32_f16 v[106:109], v[186:189], v[158:161], v[106:109]
	v_mfma_f32_16x16x32_f16 v[98:101], v[194:197], v[158:161], v[98:101]
	v_mfma_f32_16x16x32_f16 v[90:93], v[186:189], v[150:153], v[90:93]
	v_mfma_f32_16x16x32_f16 v[78:81], v[194:197], v[150:153], v[78:81]
	v_mfma_f32_16x16x32_f16 v[130:133], v[190:193], v[178:181], v[130:133]
	v_mfma_f32_16x16x32_f16 v[126:129], v[198:201], v[178:181], v[126:129]
	v_mfma_f32_16x16x32_f16 v[122:125], v[190:193], v[170:173], v[122:125]
	v_mfma_f32_16x16x32_f16 v[114:117], v[198:201], v[170:173], v[114:117]
	v_mfma_f32_16x16x32_f16 v[106:109], v[190:193], v[162:165], v[106:109]
	v_mfma_f32_16x16x32_f16 v[98:101], v[198:201], v[162:165], v[98:101]
	v_mfma_f32_16x16x32_f16 v[90:93], v[190:193], v[154:157], v[90:93]
	v_mfma_f32_16x16x32_f16 v[78:81], v[198:201], v[154:157], v[78:81]
	s_setprio 0
	s_mov_b32 m0, s54
	s_barrier
	ds_read_b128 v[150:153], v235 offset:16384
	ds_read_b128 v[154:157], v235 offset:17408
	ds_read_b128 v[158:161], v235 offset:18432
	ds_read_b128 v[162:165], v235 offset:19456
	ds_read_b128 v[166:169], v235 offset:20480
	ds_read_b128 v[170:173], v235 offset:21504
	ds_read_b128 v[174:177], v235 offset:22528
	ds_read_b128 v[178:181], v235 offset:23552
	global_load_lds_dwordx4 v216, s[44:45]
	s_mov_b32 m0, s57
	s_nop 0
	global_load_lds_dwordx4 v222, s[44:45]
	s_barrier
	s_waitcnt lgkmcnt(0)
	s_setprio 1
	s_waitcnt lgkmcnt(0)
	v_mfma_f32_16x16x32_f16 v[70:73], v[134:137], v[150:153], v[70:73]
	v_mfma_f32_16x16x32_f16 v[58:61], v[142:145], v[150:153], v[58:61]
	v_mfma_f32_16x16x32_f16 v[46:49], v[134:137], v[158:161], v[46:49]
	v_mfma_f32_16x16x32_f16 v[34:37], v[142:145], v[158:161], v[34:37]
	v_mfma_f32_16x16x32_f16 v[26:29], v[134:137], v[166:169], v[26:29]
	v_mfma_f32_16x16x32_f16 v[18:21], v[142:145], v[166:169], v[18:21]
	v_mfma_f32_16x16x32_f16 v[10:13], v[134:137], v[174:177], v[10:13]
	v_mfma_f32_16x16x32_f16 v[6:9], v[142:145], v[174:177], v[6:9]
	v_mfma_f32_16x16x32_f16 v[70:73], v[138:141], v[154:157], v[70:73]
	v_mfma_f32_16x16x32_f16 v[58:61], v[146:149], v[154:157], v[58:61]
	v_mfma_f32_16x16x32_f16 v[46:49], v[138:141], v[162:165], v[46:49]
	v_mfma_f32_16x16x32_f16 v[34:37], v[146:149], v[162:165], v[34:37]
	v_mfma_f32_16x16x32_f16 v[26:29], v[138:141], v[170:173], v[26:29]
	v_mfma_f32_16x16x32_f16 v[18:21], v[146:149], v[170:173], v[18:21]
	v_mfma_f32_16x16x32_f16 v[10:13], v[138:141], v[178:181], v[10:13]
	v_mfma_f32_16x16x32_f16 v[6:9], v[146:149], v[178:181], v[6:9]
	s_setprio 0
	s_barrier
	s_add_u32 s86, s40, 0x40000
	s_addc_u32 s87, s41, 0
	s_mov_b32 m0, s80
	v_lshl_add_u64 v[134:135], s[86:87], 0, v[212:213]
	global_load_lds_dwordx4 v[134:135], off
	v_lshl_add_u64 v[134:135], s[86:87], 0, v[214:215]
	s_mov_b32 m0, s81
	s_nop 0
	global_load_lds_dwordx4 v[134:135], off
	s_add_i32 s92, s71, s63
	s_mov_b32 s93, 0
	s_lshl_b64 s[90:91], s[92:93], 12
	s_add_i32 s92, s63, s33
	s_lshl_b64 s[92:93], s[92:93], 13
	s_add_i32 s94, s63, -1
	s_cmp_lt_u32 s94, 43
	s_waitcnt vmcnt(6)
	s_cbranch_scc0 .Lhkb_rare_b2
	v_cvt_pk_f16_f32 v2, v2, v3
	v_cvt_pk_f16_f32 v3, v4, v5
	v_lshl_add_u64 v[4:5], v[220:221], 0, s[90:91]
	global_store_dwordx2 v[4:5], v[2:3], off
	v_lshl_add_u64 v[4:5], v[224:225], 0, s[92:93]
	global_load_dwordx4 v[2:5], v[4:5], off nt
	s_add_i32 s63, s63, 1

.LBB5_46:
	s_mov_b32 m0, s62
	v_lshl_add_u64 v[182:183], v[182:183], 0, s[26:27]
	ds_read_b128 v[190:193], v236
	ds_read_b128 v[194:197], v236 offset:1024
	ds_read_b128 v[198:201], v236 offset:2048
	ds_read_b128 v[202:205], v236 offset:3072
	global_load_lds_dwordx4 v[182:183], off
	v_lshl_add_u64 v[182:183], v[184:185], 0, s[26:27]
	s_mov_b32 m0, s64
	v_mov_b32_e32 v223, v217
	global_load_lds_dwordx4 v[182:183], off
	s_barrier
	s_waitcnt lgkmcnt(0)
	v_lshl_add_u64 v[186:187], s[44:45], 0, v[216:217]
	v_lshl_add_u64 v[188:189], s[44:45], 0, v[222:223]
	s_setprio 1
	s_waitcnt lgkmcnt(0)
	v_mfma_f32_16x16x32_f16 v[130:133], v[190:193], v[174:177], v[130:133]
	v_mfma_f32_16x16x32_f16 v[126:129], v[198:201], v[174:177], v[126:129]
	v_mfma_f32_16x16x32_f16 v[122:125], v[190:193], v[166:169], v[122:125]
	v_mfma_f32_16x16x32_f16 v[114:117], v[198:201], v[166:169], v[114:117]
	v_mfma_f32_16x16x32_f16 v[106:109], v[190:193], v[158:161], v[106:109]
	v_mfma_f32_16x16x32_f16 v[98:101], v[198:201], v[158:161], v[98:101]
	v_mfma_f32_16x16x32_f16 v[90:93], v[190:193], v[150:153], v[90:93]
	v_mfma_f32_16x16x32_f16 v[78:81], v[198:201], v[150:153], v[78:81]
	v_mfma_f32_16x16x32_f16 v[130:133], v[194:197], v[178:181], v[130:133]
	v_mfma_f32_16x16x32_f16 v[126:129], v[202:205], v[178:181], v[126:129]
	v_mfma_f32_16x16x32_f16 v[122:125], v[194:197], v[170:173], v[122:125]
	v_mfma_f32_16x16x32_f16 v[114:117], v[202:205], v[170:173], v[114:117]
	v_mfma_f32_16x16x32_f16 v[106:109], v[194:197], v[162:165], v[106:109]
	v_mfma_f32_16x16x32_f16 v[98:101], v[202:205], v[162:165], v[98:101]
	v_mfma_f32_16x16x32_f16 v[90:93], v[194:197], v[154:157], v[90:93]
	v_mfma_f32_16x16x32_f16 v[78:81], v[202:205], v[154:157], v[78:81]
	s_setprio 0
	s_mov_b32 m0, s65
	v_lshl_add_u64 v[182:183], v[186:187], 0, s[26:27]
	s_barrier
	ds_read_b128 v[150:153], v235 offset:49152
	ds_read_b128 v[154:157], v235 offset:50176
	ds_read_b128 v[158:161], v235 offset:51200
	ds_read_b128 v[162:165], v235 offset:52224
	ds_read_b128 v[166:169], v235 offset:53248
	ds_read_b128 v[170:173], v235 offset:54272
	ds_read_b128 v[174:177], v235 offset:55296
	ds_read_b128 v[178:181], v235 offset:56320
	global_load_lds_dwordx4 v[182:183], off
	v_lshl_add_u64 v[182:183], v[188:189], 0, s[26:27]
	s_mov_b32 m0, s66
	s_nop 0
	global_load_lds_dwordx4 v[182:183], off
	s_barrier
	s_waitcnt lgkmcnt(0)
	s_setprio 1
	s_waitcnt lgkmcnt(0)
	v_mfma_f32_16x16x32_f16 v[70:73], v[134:137], v[150:153], v[70:73]
	v_mfma_f32_16x16x32_f16 v[58:61], v[142:145], v[150:153], v[58:61]
	v_mfma_f32_16x16x32_f16 v[46:49], v[134:137], v[158:161], v[46:49]
	v_mfma_f32_16x16x32_f16 v[34:37], v[142:145], v[158:161], v[34:37]
	v_mfma_f32_16x16x32_f16 v[26:29], v[134:137], v[166:169], v[26:29]
	v_mfma_f32_16x16x32_f16 v[18:21], v[142:145], v[166:169], v[18:21]
	v_mfma_f32_16x16x32_f16 v[10:13], v[134:137], v[174:177], v[10:13]
	v_mfma_f32_16x16x32_f16 v[6:9], v[142:145], v[174:177], v[6:9]
	v_mfma_f32_16x16x32_f16 v[70:73], v[138:141], v[154:157], v[70:73]
	v_mfma_f32_16x16x32_f16 v[58:61], v[146:149], v[154:157], v[58:61]
	v_mfma_f32_16x16x32_f16 v[46:49], v[138:141], v[162:165], v[46:49]
	v_mfma_f32_16x16x32_f16 v[34:37], v[146:149], v[162:165], v[34:37]
	v_mfma_f32_16x16x32_f16 v[26:29], v[138:141], v[170:173], v[26:29]
	v_mfma_f32_16x16x32_f16 v[18:21], v[146:149], v[170:173], v[18:21]
	v_mfma_f32_16x16x32_f16 v[10:13], v[138:141], v[178:181], v[10:13]
	v_mfma_f32_16x16x32_f16 v[6:9], v[146:149], v[178:181], v[6:9]
	s_setprio 0
	s_barrier
	s_add_u32 s40, s40, 0x40080
	s_addc_u32 s41, s41, 0
	s_mov_b32 m0, s46
	v_lshl_add_u64 v[134:135], s[40:41], 0, v[212:213]
	global_load_lds_dwordx4 v[134:135], off
	v_lshl_add_u64 v[134:135], s[40:41], 0, v[214:215]
	s_mov_b32 m0, s47
	s_nop 0
	global_load_lds_dwordx4 v[134:135], off
	s_add_i32 s92, s71, s63
	s_mov_b32 s93, 0
	s_lshl_b64 s[90:91], s[92:93], 12
	s_add_i32 s92, s63, s33
	s_lshl_b64 s[92:93], s[92:93], 13
	s_add_i32 s24, s84, 2
	s_add_u32 s42, s42, 0x100
	s_addc_u32 s43, s43, 0
	s_add_u32 s82, s82, 0x100
	s_addc_u32 s83, s83, 0
	s_add_i32 s94, s63, -1
	s_cmp_lt_u32 s94, 43
	s_waitcnt vmcnt(6)
	s_cbranch_scc0 .Lhkb_rare_b3
	v_cvt_pk_f16_f32 v2, v2, v3
	v_cvt_pk_f16_f32 v3, v4, v5
	v_lshl_add_u64 v[4:5], v[220:221], 0, s[90:91]
	global_store_dwordx2 v[4:5], v[2:3], off
	v_lshl_add_u64 v[4:5], v[224:225], 0, s[92:93]
	global_load_dwordx4 v[2:5], v[4:5], off nt
	s_add_i32 s63, s63, 1

.Lhkb_rare_b0:
	s_cmp_gt_i32 s63, 44
	s_cbranch_scc1 .Lhkb_done_b0
	s_cmp_lt_i32 s63, 1
	s_cbranch_scc1 .Lhkb_rld_b0
	v_cvt_pk_f16_f32 v2, v2, v3
	v_cvt_pk_f16_f32 v3, v4, v5
	v_lshl_add_u64 v[4:5], v[220:221], 0, s[90:91]
	global_store_dwordx2 v[4:5], v[2:3], off

.Lhkb_rinc_b0:
	s_add_i32 s63, s63, 1
	s_branch .Lhkb_done_b0

.Lhkb_rinc_b3:
	s_add_i32 s63, s63, 1
	s_branch .Lhkb_done_b3
	.p2align	8

amdhsa.kernels:
  - .agpr_count:     0
    .args:
      - .actual_access:  read_only
        .address_space:  global
        .offset:         0
        .size:           8
        .value_kind:     global_buffer
      - .actual_access:  read_only
        .address_space:  global
        .offset:         8
        .size:           8
        .value_kind:     global_buffer
      - .actual_access:  write_only
        .address_space:  global
        .offset:         16
        .size:           8
        .value_kind:     global_buffer
      - .actual_access:  write_only
        .address_space:  global
        .offset:         24
        .size:           8
        .value_kind:     global_buffer
      - .actual_access:  write_only
        .address_space:  global
        .offset:         32
        .size:           8
        .value_kind:     global_buffer
      - .actual_access:  write_only
        .address_space:  global
        .offset:         40
        .size:           8
        .value_kind:     global_buffer
    .group_segment_fixed_size: 256
    .kernarg_segment_align: 8
    .kernarg_segment_size: 48
    .language:       OpenCL C
    .language_version:
      - 2
      - 0
    .max_flat_workgroup_size: 256
    .name:           _Z10k_xscatterPKiS0_P15HIP_vector_typeIiLj2EEPtP4MetaS3_
    .private_segment_fixed_size: 0
    .sgpr_count:     41
    .sgpr_spill_count: 0
    .symbol:         _Z10k_xscatterPKiS0_P15HIP_vector_typeIiLj2EEPtP4MetaS3_.kd
    .uniform_work_group_size: 1
    .uses_dynamic_stack: false
    .vgpr_count:     55
    .vgpr_spill_count: 0
    .wavefront_size: 64
  - .agpr_count:     0
    .args:
      - .actual_access:  read_only
        .address_space:  global
        .offset:         0
        .size:           8
        .value_kind:     global_buffer
      - .actual_access:  read_only
        .address_space:  global
        .offset:         8
        .size:           8
        .value_kind:     global_buffer
      - .actual_access:  write_only
        .address_space:  global
        .offset:         16
        .size:           8
        .value_kind:     global_buffer
      - .actual_access:  write_only
        .address_space:  global
        .offset:         24
        .size:           8
        .value_kind:     global_buffer
      - .actual_access:  write_only
        .address_space:  global
        .offset:         32
        .size:           8
        .value_kind:     global_buffer
      - .actual_access:  read_only
        .address_space:  global
        .offset:         40
        .size:           8
        .value_kind:     global_buffer
      - .actual_access:  read_only
        .address_space:  global
        .offset:         48
        .size:           8
        .value_kind:     global_buffer
      - .actual_access:  write_only
        .address_space:  global
        .offset:         56
        .size:           8
        .value_kind:     global_buffer
      - .actual_access:  write_only
        .address_space:  global
        .offset:         64
        .size:           8
        .value_kind:     global_buffer
    .group_segment_fixed_size: 4096
    .kernarg_segment_align: 8
    .kernarg_segment_size: 72
    .language:       OpenCL C
    .language_version:
      - 2
      - 0
    .max_flat_workgroup_size: 256
    .name:           _Z5k_prePKfS0_PiP15HIP_vector_typeIfLj2EES1_S0_S0_PDF16_S5_
    .private_segment_fixed_size: 0
    .sgpr_count:     42
    .sgpr_spill_count: 0
    .symbol:         _Z5k_prePKfS0_PiP15HIP_vector_typeIfLj2EES1_S0_S0_PDF16_S5_.kd
    .uniform_work_group_size: 1
    .uses_dynamic_stack: false
    .vgpr_count:     128
    .vgpr_spill_count: 0
    .wavefront_size: 64
  - .agpr_count:     0
    .args:
      - .address_space:  global
        .offset:         0
        .size:           8
        .value_kind:     global_buffer
      - .address_space:  global
        .offset:         8
        .size:           8
        .value_kind:     global_buffer
      - .actual_access:  write_only
        .address_space:  global
        .offset:         16
        .size:           8
        .value_kind:     global_buffer
      - .actual_access:  read_only
        .address_space:  global
        .offset:         24
        .size:           8
        .value_kind:     global_buffer
    .group_segment_fixed_size: 0
    .kernarg_segment_align: 8
    .kernarg_segment_size: 32
    .language:       OpenCL C
    .language_version:
      - 2
      - 0
    .max_flat_workgroup_size: 512
    .name:           _Z7k_gemm2PKDF16_S0_PDF16_PK15HIP_vector_typeIiLj2EE
    .private_segment_fixed_size: 0
    .sgpr_count:     74
    .sgpr_spill_count: 0
    .symbol:         _Z7k_gemm2PKDF16_S0_PDF16_PK15HIP_vector_typeIiLj2EE.kd
    .uniform_work_group_size: 1
    .uses_dynamic_stack: false
    .vgpr_count:     226
    .vgpr_spill_count: 0
    .wavefront_size: 64
  - .agpr_count:     0
    .args:
      - .actual_access:  read_only
        .address_space:  global
        .offset:         0
        .size:           8
        .value_kind:     global_buffer
      - .actual_access:  read_only
        .address_space:  global
        .offset:         8
        .size:           8
        .value_kind:     global_buffer
      - .actual_access:  read_only
        .address_space:  global
        .offset:         16
        .size:           8
        .value_kind:     global_buffer
      - .actual_access:  write_only
        .address_space:  global
        .offset:         24
        .size:           8
        .value_kind:     global_buffer
    .group_segment_fixed_size: 0
    .kernarg_segment_align: 8
    .kernarg_segment_size: 32
    .language:       OpenCL C
    .language_version:
      - 2
      - 0
    .max_flat_workgroup_size: 256
    .name:           _Z9k_combinePKDF16_PK15HIP_vector_typeIiLj2EEPKS1_IfLj2EEPf
    .private_segment_fixed_size: 0
    .sgpr_count:     30
    .sgpr_spill_count: 0
    .symbol:         _Z9k_combinePKDF16_PK15HIP_vector_typeIiLj2EEPKS1_IfLj2EEPf.kd
    .uniform_work_group_size: 1
    .uses_dynamic_stack: false
    .vgpr_count:     64
    .vgpr_spill_count: 0
    .wavefront_size: 64
  - .agpr_count:     0
    .args:
      - .address_space:  global
        .offset:         0
        .size:           8
        .value_kind:     global_buffer
      - .address_space:  global
        .offset:         8
        .size:           8
        .value_kind:     global_buffer
      - .actual_access:  write_only
        .address_space:  global
        .offset:         16
        .size:           8
        .value_kind:     global_buffer
      - .actual_access:  read_only
        .address_space:  global
        .offset:         24
        .size:           8
        .value_kind:     global_buffer
      - .address_space:  global
        .offset:         32
        .size:           8
        .value_kind:     global_buffer
      - .address_space:  global
        .offset:         40
        .size:           8
        .value_kind:     global_buffer
      - .actual_access:  write_only
        .address_space:  global
        .offset:         48
        .size:           8
        .value_kind:     global_buffer
      - .address_space:  global
        .offset:         56
        .size:           8
        .value_kind:     global_buffer
    .group_segment_fixed_size: 0
    .kernarg_segment_align: 8
    .kernarg_segment_size: 64
    .language:       OpenCL C
    .language_version:
      - 2
      - 0
    .max_flat_workgroup_size: 512
    .name:           _Z7k_gemm1ILi0EEvPKDF16_S1_PDF16_PK15HIP_vector_typeIiLj2EEPKfS8_S2_PKt
    .private_segment_fixed_size: 0
    .sgpr_count:     108
    .sgpr_spill_count: 0
    .symbol:         _Z7k_gemm1ILi0EEvPKDF16_S1_PDF16_PK15HIP_vector_typeIiLj2EEPKfS8_S2_PKt.kd
    .uniform_work_group_size: 1
    .uses_dynamic_stack: false
    .vgpr_count:     256
    .vgpr_spill_count: 0
    .wavefront_size: 64
  - .agpr_count:     0
    .args:
      - .address_space:  global
        .offset:         0
        .size:           8
        .value_kind:     global_buffer
      - .address_space:  global
        .offset:         8
        .size:           8
        .value_kind:     global_buffer
      - .actual_access:  write_only
        .address_space:  global
        .offset:         16
        .size:           8
        .value_kind:     global_buffer
      - .actual_access:  read_only
        .address_space:  global
        .offset:         24
        .size:           8
        .value_kind:     global_buffer
      - .address_space:  global
        .offset:         32
        .size:           8
        .value_kind:     global_buffer
      - .actual_access:  read_only
        .address_space:  global
        .offset:         40
        .size:           8
        .value_kind:     global_buffer
      - .actual_access:  write_only
        .address_space:  global
        .offset:         48
        .size:           8
        .value_kind:     global_buffer
      - .address_space:  global
        .offset:         56
        .size:           8
        .value_kind:     global_buffer
    .group_segment_fixed_size: 0
    .kernarg_segment_align: 8
    .kernarg_segment_size: 64
    .language:       OpenCL C
    .language_version:
      - 2
      - 0
    .max_flat_workgroup_size: 512
    .name:           _Z7k_gemm1ILi1EEvPKDF16_S1_PDF16_PK15HIP_vector_typeIiLj2EEPKfS8_S2_PKt
    .private_segment_fixed_size: 0
    .sgpr_count:     102
    .sgpr_spill_count: 0
    .symbol:         _Z7k_gemm1ILi1EEvPKDF16_S1_PDF16_PK15HIP_vector_typeIiLj2EEPKfS8_S2_PKt.kd
    .uniform_work_group_size: 1
    .uses_dynamic_stack: false
    .vgpr_count:     254
    .vgpr_spill_count: 0
    .wavefront_size: 64
